# DSA indexer prologue de-serialised: early vmcnt(0) dropped, first four key tiles requested with the query/weight loads into spare registers and copied
# baseline (speedup 1.0000x reference)
; __device__ __forceinline__ void dsa2_unit(LAS unsigned char* lds, const bf16* PROJ, const bf16* KIDX, const bf16* KVN, bf16* OLAT, float* sbuf, int b, int t0, int tid) {
;     ...
;         { const int ntiles = (t0 >> 5) + 1, tpw = (ntiles + 7) >> 3, tile0 = wave * tpw; int tile1 = tile0 + tpw; tile1 = tile1 < ntiles ? tile1 : ntiles;
;           const int ahead = (r & 3) + 4 * ((r >> 3) & 1), atok = ((r >> 2) & 1) + 2 * (r >> 4);
;           const bf16* qpa = PROJ + (rowb + t0 + atok) * NP + PC_QIDX + ahead * 32 + 8 * h; const bf16* qpb = qpa + (size_t)4 * NP;
;           const bf16x8 A0a = *(const bf16x8*)qpa, A1a = *(const bf16x8*)(qpa + 16), A0b = *(const bf16x8*)qpb, A1b = *(const bf16x8*)(qpb + 16);
;           float wq[32];
; #pragma unroll
;           for (int gq = 0; gq < 4; ++gq) { const v4u w0 = *(const v4u*)(PROJ + (rowb + t0 + h + 2 * gq) * NP + PC_WIDX);
;               wq[8 * gq] = 0.5f * bflo(w0.x); wq[8 * gq + 1] = 0.5f * bfhi(w0.x); wq[8 * gq + 2] = 0.5f * bflo(w0.y); wq[8 * gq + 3] = 0.5f * bfhi(w0.y); wq[8 * gq + 4] = 0.5f * bflo(w0.z); wq[8 * gq + 5] = 0.5f * bfhi(w0.z); wq[8 * gq + 6] = 0.5f * bflo(w0.w); wq[8 * gq + 7] = 0.5f * bfhi(w0.w); }
;           v4u A0c = {0u, 0u, 0u, 0u}, A1c = {0u, 0u, 0u, 0u};
;           if (r < 8) { const bf16* qrow = PROJ + (rowb + t0 + (r >> 2) + 2 * (r & 3)) * NP; const v4u wv = *(const v4u*)(qrow + PC_WIDX);
.LBB0_703:
	s_lshl_b32 s5, s1, 13
	s_andn2_b64 vcc, exec, s[2:3]
	s_and_b32 s22, s5, 0x2000
	s_cbranch_vccnz .LBB0_2532
	v_and_b32_e32 v28, 31, v150
	v_and_b32_e32 v16, 3, v150
	v_lshrrev_b32_e32 v0, 1, v150
	v_lshrrev_b32_e32 v1, 3, v150
	s_waitcnt lgkmcnt(0)
	v_and_or_b32 v2, v0, 4, v16
	v_bfe_u32 v0, v28, 2, 1
	v_and_b32_e32 v1, 2, v1
	s_add_i32 s4, s22, s4
	v_or3_b32 v0, v1, v0, s4
	v_mov_b32_e32 v1, v128
	v_lshlrev_b64 v[0:1], 14, v[0:1]
	v_lshrrev_b32_e32 v29, 5, v129
	v_lshl_add_u64 v[0:1], s[74:75], 0, v[0:1]
	v_lshlrev_b32_e32 v2, 6, v2
	v_mov_b32_e32 v3, v128
	v_lshl_add_u64 v[0:1], v[0:1], 0, v[2:3]
	v_lshlrev_b32_e32 v2, 4, v29
	v_lshl_add_u64 v[0:1], v[0:1], 0, v[2:3]
	global_load_dwordx4 v[56:59], v[0:1], off offset:2560
	global_load_dwordx4 v[48:51], v[0:1], off offset:2592
	v_add_co_u32_e32 v0, vcc, s95, v0
	v_lshlrev_b32_e32 v17, 3, v29
	s_nop 0
	v_addc_co_u32_e32 v1, vcc, 0, v1, vcc
	global_load_dwordx4 v[60:63], v[0:1], off offset:2560
	global_load_dwordx4 v[52:55], v[0:1], off offset:2592
	v_or_b32_e32 v0, s4, v29
	v_mov_b32_e32 v1, v128
	v_lshlrev_b64 v[0:1], 14, v[0:1]
	v_lshl_add_u64 v[0:1], s[74:75], 0, v[0:1]
	v_add_co_u32_e32 v2, vcc, 0x8000, v0
	v_mov_b32_e32 v68, 0
	v_addc_co_u32_e32 v3, vcc, 0, v1, vcc
	global_load_dwordx4 v[12:15], v[0:1], off offset:2368
	global_load_dwordx4 v[8:11], v[2:3], off offset:2368
	v_add_co_u32_e32 v2, vcc, 0x10000, v0
	v_lshlrev_b32_e32 v24, 1, v17
	s_nop 0
	v_addc_co_u32_e32 v3, vcc, 0, v1, vcc
	v_add_co_u32_e32 v0, vcc, 0x18000, v0
	v_mov_b32_e32 v69, v68
	s_nop 0
	v_addc_co_u32_e32 v1, vcc, 0, v1, vcc
	global_load_dwordx4 v[4:7], v[2:3], off offset:2368
	s_nop 0
	global_load_dwordx4 v[0:3], v[0:1], off offset:2368
	s_lshr_b32 s59, s1, 3
	s_add_i32 s63, s59, 8
	s_lshr_b32 s63, s63, 3
	s_mul_i32 s66, s0, s63
	s_add_i32 s84, s66, s63
	s_add_i32 s59, s59, 1
	s_min_i32 s84, s84, s59
	s_cmp_ge_i32 s66, s84
	s_cbranch_scc1 .Lidx_nopre
	s_lshl_b32 s85, s66, 5
	s_add_i32 s85, s85, s22
	s_sub_i32 s84, s84, 1
	v_or_b32_e32 v228, s85, v28
	v_mov_b32_e32 v229, 0
	v_lshlrev_b64 v[228:229], 6, v[228:229]
	v_mov_b32_e32 v230, v24
	v_mov_b32_e32 v231, 0
	v_lshl_add_u64 v[228:229], s[78:79], 0, v[228:229]
	v_lshl_add_u64 v[228:229], v[228:229], 0, v[230:231]
	s_mov_b32 s87, 0
	global_load_dwordx4 v[188:191], v[228:229], off
	global_load_dwordx4 v[192:195], v[228:229], off offset:32
	s_add_i32 s86, s66, 1
	s_min_i32 s86, s86, s84
	s_sub_i32 s86, s86, s66
	s_lshl_b32 s86, s86, 11
	v_lshl_add_u64 v[232:233], v[228:229], 0, s[86:87]
	global_load_dwordx4 v[196:199], v[232:233], off
	global_load_dwordx4 v[200:203], v[232:233], off offset:32
	s_add_i32 s86, s66, 2
	s_min_i32 s86, s86, s84
	s_sub_i32 s86, s86, s66
	s_lshl_b32 s86, s86, 11
	v_lshl_add_u64 v[232:233], v[228:229], 0, s[86:87]
	global_load_dwordx4 v[204:207], v[232:233], off
	global_load_dwordx4 v[208:211], v[232:233], off offset:32
	s_add_i32 s86, s66, 3
	s_min_i32 s86, s86, s84
	s_sub_i32 s86, s86, s66
	s_lshl_b32 s86, s86, 11
	v_lshl_add_u64 v[232:233], v[228:229], 0, s[86:87]
	global_load_dwordx4 v[220:223], v[232:233], off
	global_load_dwordx4 v[224:227], v[232:233], off offset:32
.Lidx_nopre:
	v_cmp_gt_u32_e32 vcc, 8, v28
	v_mov_b32_e32 v70, v68
	v_mov_b32_e32 v71, v68
	v_mov_b32_e32 v64, v68
	v_mov_b32_e32 v65, v68
	v_mov_b32_e32 v66, v68
	v_mov_b32_e32 v67, v68
	s_and_saveexec_b64 s[2:3], vcc
	s_cbranch_execz .LBB0_706
	v_bfe_u32 v17, v150, 2, 3
	v_lshlrev_b32_e32 v16, 1, v16
	v_or3_b32 v16, v16, s4, v17
	v_mov_b32_e32 v17, v128
	v_lshlrev_b64 v[16:17], 14, v[16:17]
	v_lshl_add_u64 v[16:17], s[74:75], 0, v[16:17]
	global_load_dwordx4 v[30:33], v[16:17], off offset:2368
	v_mov_b32_e32 v25, v128
	v_lshl_add_u64 v[26:27], v[16:17], 0, v[24:25]
	global_load_dwordx4 v[34:37], v[26:27], off offset:2560
	global_load_dwordx4 v[38:41], v[26:27], off offset:2624
	global_load_dwordx4 v[42:45], v[26:27], off offset:2592
	global_load_dwordx4 v[64:67], v[26:27], off offset:2656
	global_load_dwordx4 v[68:71], v[26:27], off offset:2688
	global_load_dwordx4 v[72:75], v[26:27], off offset:2720
	global_load_dwordx4 v[76:79], v[26:27], off offset:2752
	global_load_dwordx4 v[80:83], v[26:27], off offset:2784
	global_load_dwordx4 v[84:87], v[26:27], off offset:2816
	global_load_dwordx4 v[88:91], v[26:27], off offset:2848
	global_load_dwordx4 v[92:95], v[26:27], off offset:2880
	global_load_dwordx4 v[20:23], v[26:27], off offset:2912
	global_load_dwordx4 v[96:99], v[26:27], off offset:2944
	global_load_dwordx4 v[16:19], v[26:27], off offset:2976
	global_load_dwordx4 v[100:103], v[26:27], off offset:3008
	s_waitcnt vmcnt(0)
; __device__ __forceinline__ void dsa2_unit(LAS unsigned char* lds, const bf16* PROJ, const bf16* KIDX, const bf16* KVN, bf16* OLAT, float* sbuf, int b, int t0, int tid) {
;     ...
;           if (r < 8) { const bf16* qrow = PROJ + (rowb + t0 + (r >> 2) + 2 * (r & 3)) * NP; const v4u wv = *(const v4u*)(qrow + PC_WIDX);
;               const float wl_[8] = {bflo(wv.x), bfhi(wv.x), bflo(wv.y), bfhi(wv.y), bflo(wv.z), bfhi(wv.z), bflo(wv.w), bfhi(wv.w)};
;               float a0[8], a1[8];
; #pragma unroll
;               for (int j = 0; j < 8; ++j) { a0[j] = 0.f; a1[j] = 0.f; }
; #pragma unroll
;               for (int hd = 0; hd < 8; ++hd) { const v4u q0 = *(const v4u*)(qrow + PC_QIDX + hd * 32 + 8 * h), q1 = *(const v4u*)(qrow + PC_QIDX + hd * 32 + 16 + 8 * h); const float hw = 0.5f * wl_[hd];
;                   a0[0] += hw * bflo(q0.x); a0[1] += hw * bfhi(q0.x); a0[2] += hw * bflo(q0.y); a0[3] += hw * bfhi(q0.y); a0[4] += hw * bflo(q0.z); a0[5] += hw * bfhi(q0.z); a0[6] += hw * bflo(q0.w); a0[7] += hw * bfhi(q0.w);
;                   a1[0] += hw * bflo(q1.x); a1[1] += hw * bfhi(q1.x); a1[2] += hw * bflo(q1.y); a1[3] += hw * bfhi(q1.y); a1[4] += hw * bflo(q1.z); a1[5] += hw * bfhi(q1.z); a1[6] += hw * bflo(q1.w); a1[7] += hw * bfhi(q1.w); }
	v_lshlrev_b32_e32 v47, 16, v35
	v_and_b32_e32 v35, 0xffff0000, v35
	v_lshlrev_b32_e32 v107, 16, v37
	v_lshlrev_b32_e32 v106, 16, v36
	v_and_b32_e32 v37, 0xffff0000, v37
	v_and_b32_e32 v36, 0xffff0000, v36
	v_lshlrev_b32_e32 v111, 16, v43
	v_lshlrev_b32_e32 v110, 16, v42
	v_and_b32_e32 v43, 0xffff0000, v43
	v_and_b32_e32 v42, 0xffff0000, v42
	v_lshlrev_b32_e32 v115, 16, v45
	v_lshlrev_b32_e32 v25, 16, v30
	v_and_b32_e32 v46, 0xffff0000, v30
	v_lshlrev_b32_e32 v124, 16, v32
	v_and_b32_e32 v134, 0xffff0000, v32
	v_mul_f32_e32 v30, 0.5, v25
	v_mul_f32_e32 v32, 0.5, v46
	v_lshlrev_b32_e32 v46, 16, v34
	v_and_b32_e32 v34, 0xffff0000, v34
	v_lshlrev_b32_e32 v114, 16, v44
	v_and_b32_e32 v45, 0xffff0000, v45
	v_and_b32_e32 v44, 0xffff0000, v44
	v_lshlrev_b32_e32 v118, 16, v31
	v_and_b32_e32 v119, 0xffff0000, v31
	v_lshlrev_b32_e32 v105, 16, v39
	v_lshlrev_b32_e32 v104, 16, v38
	v_and_b32_e32 v39, 0xffff0000, v39
	v_and_b32_e32 v38, 0xffff0000, v38
	v_lshlrev_b32_e32 v109, 16, v41
	v_lshlrev_b32_e32 v108, 16, v40
	v_and_b32_e32 v41, 0xffff0000, v41
	v_and_b32_e32 v40, 0xffff0000, v40
	v_lshlrev_b32_e32 v113, 16, v65
	v_lshlrev_b32_e32 v112, 16, v64
	v_and_b32_e32 v65, 0xffff0000, v65
	v_and_b32_e32 v64, 0xffff0000, v64
	v_lshlrev_b32_e32 v117, 16, v67
	v_lshlrev_b32_e32 v116, 16, v66
	v_and_b32_e32 v67, 0xffff0000, v67
	v_and_b32_e32 v66, 0xffff0000, v66
	v_pk_fma_f32 v[46:47], v[30:31], v[46:47], 0 op_sel_hi:[0,1,0]
	v_pk_fma_f32 v[34:35], v[30:31], v[34:35], 0 op_sel_hi:[0,1,0]
	v_pk_fma_f32 v[106:107], v[30:31], v[106:107], 0 op_sel_hi:[0,1,0]
	v_pk_fma_f32 v[36:37], v[30:31], v[36:37], 0 op_sel_hi:[0,1,0]
	v_pk_fma_f32 v[110:111], v[30:31], v[110:111], 0 op_sel_hi:[0,1,0]
	v_pk_fma_f32 v[42:43], v[30:31], v[42:43], 0 op_sel_hi:[0,1,0]
	v_pk_fma_f32 v[114:115], v[30:31], v[114:115], 0 op_sel_hi:[0,1,0]
	v_pk_fma_f32 v[30:31], v[30:31], v[44:45], 0 op_sel_hi:[0,1,0]
	v_lshlrev_b32_e32 v135, 16, v33
	v_and_b32_e32 v137, 0xffff0000, v33
	v_pk_fma_f32 v[44:45], v[32:33], v[104:105], v[46:47] op_sel_hi:[0,1,1]
	v_pk_fma_f32 v[34:35], v[32:33], v[38:39], v[34:35] op_sel_hi:[0,1,1]
	v_pk_fma_f32 v[38:39], v[32:33], v[108:109], v[106:107] op_sel_hi:[0,1,1]
	v_pk_fma_f32 v[36:37], v[32:33], v[40:41], v[36:37] op_sel_hi:[0,1,1]
	v_pk_fma_f32 v[40:41], v[32:33], v[112:113], v[110:111] op_sel_hi:[0,1,1]
	v_pk_fma_f32 v[42:43], v[32:33], v[64:65], v[42:43] op_sel_hi:[0,1,1]
	v_pk_fma_f32 v[46:47], v[32:33], v[116:117], v[114:115] op_sel_hi:[0,1,1]
	v_pk_fma_f32 v[104:105], v[32:33], v[66:67], v[30:31] op_sel_hi:[0,1,1]
	global_load_dwordx4 v[30:33], v[26:27], off offset:3040
	v_mul_f32_e32 v118, 0.5, v118
	v_lshlrev_b32_e32 v121, 16, v69
	v_lshlrev_b32_e32 v120, 16, v68
	v_and_b32_e32 v69, 0xffff0000, v69
	v_and_b32_e32 v68, 0xffff0000, v68
	v_lshlrev_b32_e32 v123, 16, v71
	v_lshlrev_b32_e32 v122, 16, v70
	v_mul_f32_e32 v108, 0.5, v119
	v_lshlrev_b32_e32 v67, 16, v77
	v_lshlrev_b32_e32 v66, 16, v76
	v_pk_fma_f32 v[44:45], v[118:119], v[120:121], v[44:45] op_sel_hi:[0,1,1]
	v_and_b32_e32 v65, 0xffff0000, v71
	v_and_b32_e32 v64, 0xffff0000, v70
	v_and_b32_e32 v77, 0xffff0000, v77
	v_and_b32_e32 v76, 0xffff0000, v76
	v_lshlrev_b32_e32 v111, 16, v79
	v_lshlrev_b32_e32 v110, 16, v78
	v_mul_f32_e32 v116, 0.5, v124
	v_lshlrev_b32_e32 v124, 16, v84
	v_lshlrev_b32_e32 v125, 16, v85
	v_pk_fma_f32 v[34:35], v[118:119], v[68:69], v[34:35] op_sel_hi:[0,1,1]
	v_pk_fma_f32 v[44:45], v[108:109], v[66:67], v[44:45] op_sel_hi:[0,1,1]
	v_pk_fma_f32 v[38:39], v[118:119], v[122:123], v[38:39] op_sel_hi:[0,1,1]
	v_and_b32_e32 v79, 0xffff0000, v79
	v_and_b32_e32 v78, 0xffff0000, v78
	v_and_b32_e32 v84, 0xffff0000, v84
	v_and_b32_e32 v85, 0xffff0000, v85
	v_lshlrev_b32_e32 v126, 16, v86
	v_lshlrev_b32_e32 v127, 16, v87
	v_mul_f32_e32 v134, 0.5, v134
	v_pk_fma_f32 v[34:35], v[108:109], v[76:77], v[34:35] op_sel_hi:[0,1,1]
	v_pk_fma_f32 v[44:45], v[116:117], v[124:125], v[44:45] op_sel_hi:[0,1,1]
	v_lshlrev_b32_e32 v67, 16, v93
	v_lshlrev_b32_e32 v66, 16, v92
	v_pk_fma_f32 v[36:37], v[118:119], v[64:65], v[36:37] op_sel_hi:[0,1,1]
	v_pk_fma_f32 v[38:39], v[108:109], v[110:111], v[38:39] op_sel_hi:[0,1,1]
	v_and_b32_e32 v86, 0xffff0000, v86
	v_and_b32_e32 v87, 0xffff0000, v87
	v_pk_fma_f32 v[34:35], v[116:117], v[84:85], v[34:35] op_sel_hi:[0,1,1]
	v_pk_fma_f32 v[44:45], v[134:135], v[66:67], v[44:45] op_sel_hi:[0,1,1]
	v_and_b32_e32 v67, 0xffff0000, v93
	v_and_b32_e32 v66, 0xffff0000, v92
	v_pk_fma_f32 v[36:37], v[108:109], v[78:79], v[36:37] op_sel_hi:[0,1,1]
	v_pk_fma_f32 v[38:39], v[116:117], v[126:127], v[38:39] op_sel_hi:[0,1,1]
	v_lshlrev_b32_e32 v65, 16, v95
	v_lshlrev_b32_e32 v64, 16, v94
	v_mul_f32_e32 v136, 0.5, v135
	v_pk_fma_f32 v[34:35], v[134:135], v[66:67], v[34:35] op_sel_hi:[0,1,1]
	v_lshlrev_b32_e32 v67, 16, v97
	v_lshlrev_b32_e32 v66, 16, v96
	v_pk_fma_f32 v[36:37], v[116:117], v[86:87], v[36:37] op_sel_hi:[0,1,1]
	v_pk_fma_f32 v[38:39], v[134:135], v[64:65], v[38:39] op_sel_hi:[0,1,1]
	v_and_b32_e32 v65, 0xffff0000, v95
	v_and_b32_e32 v64, 0xffff0000, v94
	v_pk_fma_f32 v[44:45], v[136:137], v[66:67], v[44:45] op_sel_hi:[0,1,1]
	v_and_b32_e32 v67, 0xffff0000, v97
	v_and_b32_e32 v66, 0xffff0000, v96
	v_pk_fma_f32 v[36:37], v[134:135], v[64:65], v[36:37] op_sel_hi:[0,1,1]
	v_lshlrev_b32_e32 v65, 16, v99
	v_lshlrev_b32_e32 v64, 16, v98
	v_mul_f32_e32 v26, 0.5, v137
	v_pk_fma_f32 v[34:35], v[136:137], v[66:67], v[34:35] op_sel_hi:[0,1,1]
	v_lshlrev_b32_e32 v67, 16, v101
	v_lshlrev_b32_e32 v66, 16, v100
	v_pk_fma_f32 v[38:39], v[136:137], v[64:65], v[38:39] op_sel_hi:[0,1,1]
	v_and_b32_e32 v65, 0xffff0000, v99
	v_and_b32_e32 v64, 0xffff0000, v98
; __device__ __forceinline__ unsigned pk2(float lo, float hi) { return f2bf(lo) | (f2bf(hi) << 16); }
; __device__ __forceinline__ void dsa2_unit(LAS unsigned char* lds, const bf16* PROJ, const bf16* KIDX, const bf16* KVN, bf16* OLAT, float* sbuf, int b, int t0, int tid) {
;     ...
;               for (int hd = 0; hd < 8; ++hd) { const v4u q0 = *(const v4u*)(qrow + PC_QIDX + hd * 32 + 8 * h), q1 = *(const v4u*)(qrow + PC_QIDX + hd * 32 + 16 + 8 * h); const float hw = 0.5f * wl_[hd];
;                   a0[0] += hw * bflo(q0.x); a0[1] += hw * bfhi(q0.x); a0[2] += hw * bflo(q0.y); a0[3] += hw * bfhi(q0.y); a0[4] += hw * bflo(q0.z); a0[5] += hw * bfhi(q0.z); a0[6] += hw * bflo(q0.w); a0[7] += hw * bfhi(q0.w);
;                   a1[0] += hw * bflo(q1.x); a1[1] += hw * bfhi(q1.x); a1[2] += hw * bflo(q1.y); a1[3] += hw * bfhi(q1.y); a1[4] += hw * bflo(q1.z); a1[5] += hw * bfhi(q1.z); a1[6] += hw * bflo(q1.w); a1[7] += hw * bfhi(q1.w); }
;               A0c = (v4u){pk2(a0[0], a0[1]), pk2(a0[2], a0[3]), pk2(a0[4], a0[5]), pk2(a0[6], a0[7])}; A1c = (v4u){pk2(a1[0], a1[1]), pk2(a1[2], a1[3]), pk2(a1[4], a1[5]), pk2(a1[6], a1[7])}; }
	v_pk_fma_f32 v[44:45], v[26:27], v[66:67], v[44:45] op_sel_hi:[0,1,1]
	v_and_b32_e32 v67, 0xffff0000, v101
	v_and_b32_e32 v66, 0xffff0000, v100
	v_pk_fma_f32 v[36:37], v[136:137], v[64:65], v[36:37] op_sel_hi:[0,1,1]
	v_lshlrev_b32_e32 v65, 16, v103
	v_lshlrev_b32_e32 v64, 16, v102
	v_pk_fma_f32 v[34:35], v[26:27], v[66:67], v[34:35] op_sel_hi:[0,1,1]
	v_pk_fma_f32 v[38:39], v[26:27], v[64:65], v[38:39] op_sel_hi:[0,1,1]
	v_and_b32_e32 v65, 0xffff0000, v103
	v_and_b32_e32 v64, 0xffff0000, v102
	v_pk_fma_f32 v[36:37], v[26:27], v[64:65], v[36:37] op_sel_hi:[0,1,1]
	v_bfe_u32 v25, v34, 16, 1
	v_bfe_u32 v27, v35, 16, 1
	v_add3_u32 v27, v35, v27, s55
	v_add3_u32 v25, v34, v25, s55
	v_bfe_u32 v34, v39, 16, 1
	v_bfe_u32 v35, v38, 16, 1
	v_bfe_u32 v64, v36, 16, 1
	v_bfe_u32 v65, v37, 16, 1
	v_add3_u32 v35, v38, v35, s55
	v_add3_u32 v34, v39, v34, s55
	v_lshlrev_b32_e32 v71, 16, v73
	v_lshlrev_b32_e32 v70, 16, v72
	v_and_b32_e32 v73, 0xffff0000, v73
	v_and_b32_e32 v72, 0xffff0000, v72
	v_add3_u32 v37, v37, v65, s55
	v_add3_u32 v36, v36, v64, s55
	v_bfe_u32 v64, v45, 16, 1
	v_bfe_u32 v65, v44, 16, 1
	v_lshrrev_b32_e32 v34, 16, v34
	v_lshrrev_b32_e32 v35, 16, v35
	v_lshlrev_b32_e32 v113, 16, v81
	v_lshlrev_b32_e32 v112, 16, v80
	v_and_b32_e32 v81, 0xffff0000, v81
	v_and_b32_e32 v80, 0xffff0000, v80
	v_add3_u32 v44, v44, v65, s55
	v_add3_u32 v45, v45, v64, s55
	v_and_or_b32 v66, v36, s53, v35
	v_and_or_b32 v67, v37, s53, v34
	v_pk_fma_f32 v[34:35], v[118:119], v[70:71], v[40:41] op_sel_hi:[0,1,1]
	v_pk_fma_f32 v[36:37], v[118:119], v[72:73], v[42:43] op_sel_hi:[0,1,1]
	v_lshlrev_b32_e32 v130, 16, v88
	v_and_b32_e32 v88, 0xffff0000, v88
	v_lshlrev_b32_e32 v131, 16, v89
	v_and_b32_e32 v89, 0xffff0000, v89
	v_lshrrev_b32_e32 v38, 16, v45
	v_lshrrev_b32_e32 v39, 16, v44
	v_pk_fma_f32 v[34:35], v[108:109], v[112:113], v[34:35] op_sel_hi:[0,1,1]
	v_pk_fma_f32 v[36:37], v[108:109], v[80:81], v[36:37] op_sel_hi:[0,1,1]
	v_and_or_b32 v64, v25, s53, v39
	v_and_or_b32 v65, v27, s53, v38
	v_pk_fma_f32 v[34:35], v[116:117], v[130:131], v[34:35] op_sel_hi:[0,1,1]
	v_pk_fma_f32 v[36:37], v[116:117], v[88:89], v[36:37] op_sel_hi:[0,1,1]
	v_lshlrev_b32_e32 v39, 16, v21
	v_lshlrev_b32_e32 v38, 16, v20
	v_and_b32_e32 v21, 0xffff0000, v21
	v_and_b32_e32 v20, 0xffff0000, v20
	v_pk_fma_f32 v[34:35], v[134:135], v[38:39], v[34:35] op_sel_hi:[0,1,1]
	v_pk_fma_f32 v[20:21], v[134:135], v[20:21], v[36:37] op_sel_hi:[0,1,1]
	v_lshlrev_b32_e32 v37, 16, v17
	v_lshlrev_b32_e32 v36, 16, v16
	v_and_b32_e32 v17, 0xffff0000, v17
	v_and_b32_e32 v16, 0xffff0000, v16
	v_lshlrev_b32_e32 v107, 16, v75
	v_lshlrev_b32_e32 v106, 16, v74
	v_and_b32_e32 v75, 0xffff0000, v75
	v_and_b32_e32 v74, 0xffff0000, v74
	v_pk_fma_f32 v[34:35], v[136:137], v[36:37], v[34:35] op_sel_hi:[0,1,1]
	v_pk_fma_f32 v[16:17], v[136:137], v[16:17], v[20:21] op_sel_hi:[0,1,1]
	s_waitcnt vmcnt(0)
	v_lshlrev_b32_e32 v21, 16, v31
	v_lshlrev_b32_e32 v20, 16, v30
	v_and_b32_e32 v31, 0xffff0000, v31
	v_and_b32_e32 v30, 0xffff0000, v30
	v_lshlrev_b32_e32 v115, 16, v83
	v_lshlrev_b32_e32 v114, 16, v82
	v_and_b32_e32 v83, 0xffff0000, v83
	v_and_b32_e32 v82, 0xffff0000, v82
	v_pk_fma_f32 v[20:21], v[26:27], v[20:21], v[34:35] op_sel_hi:[0,1,1]
	v_pk_fma_f32 v[16:17], v[26:27], v[30:31], v[16:17] op_sel_hi:[0,1,1]
	v_pk_fma_f32 v[30:31], v[118:119], v[106:107], v[46:47] op_sel_hi:[0,1,1]
	v_pk_fma_f32 v[34:35], v[118:119], v[74:75], v[104:105] op_sel_hi:[0,1,1]
	v_lshlrev_b32_e32 v132, 16, v90
	v_and_b32_e32 v90, 0xffff0000, v90
	v_lshlrev_b32_e32 v133, 16, v91
	v_and_b32_e32 v91, 0xffff0000, v91
	v_pk_fma_f32 v[30:31], v[108:109], v[114:115], v[30:31] op_sel_hi:[0,1,1]
	v_pk_fma_f32 v[34:35], v[108:109], v[82:83], v[34:35] op_sel_hi:[0,1,1]
	v_pk_fma_f32 v[30:31], v[116:117], v[132:133], v[30:31] op_sel_hi:[0,1,1]
	v_pk_fma_f32 v[34:35], v[116:117], v[90:91], v[34:35] op_sel_hi:[0,1,1]
	v_lshlrev_b32_e32 v37, 16, v23
	v_lshlrev_b32_e32 v36, 16, v22
	v_and_b32_e32 v23, 0xffff0000, v23
	v_and_b32_e32 v22, 0xffff0000, v22
	v_pk_fma_f32 v[30:31], v[134:135], v[36:37], v[30:31] op_sel_hi:[0,1,1]
	v_pk_fma_f32 v[22:23], v[134:135], v[22:23], v[34:35] op_sel_hi:[0,1,1]
	v_lshlrev_b32_e32 v35, 16, v19
	v_lshlrev_b32_e32 v34, 16, v18
	v_and_b32_e32 v19, 0xffff0000, v19
	v_and_b32_e32 v18, 0xffff0000, v18
	v_pk_fma_f32 v[30:31], v[136:137], v[34:35], v[30:31] op_sel_hi:[0,1,1]
	v_pk_fma_f32 v[18:19], v[136:137], v[18:19], v[22:23] op_sel_hi:[0,1,1]
	v_lshlrev_b32_e32 v23, 16, v33
	v_lshlrev_b32_e32 v22, 16, v32
	v_pk_fma_f32 v[22:23], v[26:27], v[22:23], v[30:31] op_sel_hi:[0,1,1]
	v_and_b32_e32 v31, 0xffff0000, v33
	v_and_b32_e32 v30, 0xffff0000, v32
	v_pk_fma_f32 v[18:19], v[26:27], v[30:31], v[18:19] op_sel_hi:[0,1,1]
	v_bfe_u32 v25, v16, 16, 1
	v_bfe_u32 v26, v17, 16, 1
	v_bfe_u32 v27, v18, 16, 1
	v_bfe_u32 v30, v19, 16, 1
	v_add3_u32 v19, v19, v30, s55
	v_add3_u32 v18, v18, v27, s55
	v_add3_u32 v17, v17, v26, s55
	v_add3_u32 v16, v16, v25, s55
	v_bfe_u32 v25, v23, 16, 1
	v_bfe_u32 v26, v22, 16, 1
	v_bfe_u32 v27, v21, 16, 1
	v_bfe_u32 v30, v20, 16, 1
	v_add3_u32 v20, v20, v30, s55
	v_add3_u32 v21, v21, v27, s55
	v_add3_u32 v22, v22, v26, s55
	v_add3_u32 v23, v23, v25, s55
	v_lshrrev_b32_e32 v23, 16, v23
	v_lshrrev_b32_e32 v22, 16, v22
	v_lshrrev_b32_e32 v21, 16, v21
	v_lshrrev_b32_e32 v20, 16, v20
	v_and_or_b32 v68, v16, s53, v20
	v_and_or_b32 v69, v17, s53, v21
	v_and_or_b32 v70, v18, s53, v22
	v_and_or_b32 v71, v19, s53, v23
; __device__ __forceinline__ void dsa2_unit(LAS unsigned char* lds, const bf16* PROJ, const bf16* KIDX, const bf16* KVN, bf16* OLAT, float* sbuf, int b, int t0, int tid) {
;     ...
;         { const int ntiles = (t0 >> 5) + 1, tpw = (ntiles + 7) >> 3, tile0 = wave * tpw; int tile1 = tile0 + tpw; tile1 = tile1 < ntiles ? tile1 : ntiles;
;           const int ahead = (r & 3) + 4 * ((r >> 3) & 1), atok = ((r >> 2) & 1) + 2 * (r >> 4);
;           const bf16* qpa = PROJ + (rowb + t0 + atok) * NP + PC_QIDX + ahead * 32 + 8 * h; const bf16* qpb = qpa + (size_t)4 * NP;
;           const bf16x8 A0a = *(const bf16x8*)qpa, A1a = *(const bf16x8*)(qpa + 16), A0b = *(const bf16x8*)qpb, A1b = *(const bf16x8*)(qpb + 16);
;           float wq[32];
; #pragma unroll
;           for (int gq = 0; gq < 4; ++gq) { const v4u w0 = *(const v4u*)(PROJ + (rowb + t0 + h + 2 * gq) * NP + PC_WIDX);
;               wq[8 * gq] = 0.5f * bflo(w0.x); wq[8 * gq + 1] = 0.5f * bfhi(w0.x); wq[8 * gq + 2] = 0.5f * bflo(w0.y); wq[8 * gq + 3] = 0.5f * bfhi(w0.y); wq[8 * gq + 4] = 0.5f * bflo(w0.z); wq[8 * gq + 5] = 0.5f * bfhi(w0.z); wq[8 * gq + 6] = 0.5f * bflo(w0.w); wq[8 * gq + 7] = 0.5f * bfhi(w0.w); }
;           v4u A0c = {0u, 0u, 0u, 0u}, A1c = {0u, 0u, 0u, 0u};
;           if (r < 8) { const bf16* qrow = PROJ + (rowb + t0 + (r >> 2) + 2 * (r & 3)) * NP; const v4u wv = *(const v4u*)(qrow + PC_WIDX);
;               const float wl_[8] = {bflo(wv.x), bfhi(wv.x), bflo(wv.y), bfhi(wv.y), bflo(wv.z), bfhi(wv.z), bflo(wv.w), bfhi(wv.w)};
;               float a0[8], a1[8];
; #pragma unroll
;               for (int j = 0; j < 8; ++j) { a0[j] = 0.f; a1[j] = 0.f; }
; #pragma unroll
;               for (int hd = 0; hd < 8; ++hd) { const v4u q0 = *(const v4u*)(qrow + PC_QIDX + hd * 32 + 8 * h), q1 = *(const v4u*)(qrow + PC_QIDX + hd * 32 + 16 + 8 * h); const float hw = 0.5f * wl_[hd];
;                   a0[0] += hw * bflo(q0.x); a0[1] += hw * bfhi(q0.x); a0[2] += hw * bflo(q0.y); a0[3] += hw * bfhi(q0.y); a0[4] += hw * bflo(q0.z); a0[5] += hw * bfhi(q0.z); a0[6] += hw * bflo(q0.w); a0[7] += hw * bfhi(q0.w);
;                   a1[0] += hw * bflo(q1.x); a1[1] += hw * bfhi(q1.x); a1[2] += hw * bflo(q1.y); a1[3] += hw * bfhi(q1.y); a1[4] += hw * bflo(q1.z); a1[5] += hw * bfhi(q1.z); a1[6] += hw * bflo(q1.w); a1[7] += hw * bfhi(q1.w); }
.LBB0_706:
	s_or_b64 exec, exec, s[2:3]
	s_lshr_b32 s1, s1, 3
	s_add_i32 s2, s1, 8
	s_lshr_b32 s4, s2, 3
	s_mul_i32 s2, s0, s4
	s_add_i32 s3, s2, s4
	s_add_i32 s1, s1, 1
	v_mov_b32_e32 v139, v128
	s_min_i32 s1, s3, s1
	v_lshlrev_b64 v[16:17], 18, v[138:139]
	s_cmp_ge_i32 s2, s1
	v_lshl_add_u64 v[140:141], s[80:81], 0, v[16:17]
	s_mov_b32 s12, 0x20000
	s_mov_b32 s13, 0x30000
	s_cbranch_scc1 .LBB0_720
	s_ashr_i32 s3, s2, 31
	s_lshl_b64 s[6:7], s[2:3], 5
	s_add_u32 s3, s6, s22
	s_addc_u32 s5, s7, 0
	v_or_b32_e32 v16, s3, v28
	v_mov_b32_e32 v17, s5
	v_lshlrev_b64 v[16:17], 6, v[16:17]
	v_lshl_add_u64 v[16:17], s[78:79], 0, v[16:17]
	v_mov_b32_e32 v25, v128
	v_lshl_add_u64 v[142:143], v[16:17], 0, v[24:25]
	s_waitcnt vmcnt(0)
	v_lshlrev_b32_e32 v16, 16, v12
	v_and_b32_e32 v12, 0xffff0000, v12
	v_mul_f32_e32 v157, 0.5, v12
	v_lshlrev_b32_e32 v12, 16, v13
	v_mul_f32_e32 v155, 0.5, v12
	v_and_b32_e32 v12, 0xffff0000, v13
	v_mul_f32_e32 v154, 0.5, v12
	v_lshlrev_b32_e32 v12, 16, v14
	v_mul_f32_e32 v153, 0.5, v12
	v_and_b32_e32 v12, 0xffff0000, v14
	v_mul_f32_e32 v152, 0.5, v12
	v_lshlrev_b32_e32 v12, 16, v15
	v_mul_f32_e32 v151, 0.5, v12
	v_and_b32_e32 v12, 0xffff0000, v15
	v_mul_f32_e32 v139, 0.5, v12
	v_lshlrev_b32_e32 v12, 16, v8
	v_and_b32_e32 v8, 0xffff0000, v8
	v_mul_f32_e32 v165, 0.5, v8
	v_lshlrev_b32_e32 v8, 16, v9
	v_mul_f32_e32 v164, 0.5, v8
	v_and_b32_e32 v8, 0xffff0000, v9
	v_mul_f32_e32 v163, 0.5, v8
	v_lshlrev_b32_e32 v8, 16, v10
	v_mul_f32_e32 v162, 0.5, v8
	v_and_b32_e32 v8, 0xffff0000, v10
	v_mul_f32_e32 v161, 0.5, v8
	v_lshlrev_b32_e32 v8, 16, v11
	v_mul_f32_e32 v160, 0.5, v8
	v_and_b32_e32 v8, 0xffff0000, v11
	v_mul_f32_e32 v159, 0.5, v8
	v_lshlrev_b32_e32 v8, 16, v4
	v_and_b32_e32 v4, 0xffff0000, v4
	v_mul_f32_e32 v173, 0.5, v4
	v_lshlrev_b32_e32 v4, 16, v5
	v_mul_f32_e32 v172, 0.5, v4
	v_and_b32_e32 v4, 0xffff0000, v5
	v_mul_f32_e32 v171, 0.5, v4
	v_lshlrev_b32_e32 v4, 16, v6
	v_mul_f32_e32 v170, 0.5, v4
	v_and_b32_e32 v4, 0xffff0000, v6
	v_mul_f32_e32 v169, 0.5, v4
	v_lshlrev_b32_e32 v4, 16, v7
	v_mul_f32_e32 v168, 0.5, v4
	v_and_b32_e32 v4, 0xffff0000, v7
	v_mul_f32_e32 v167, 0.5, v4
	v_lshlrev_b32_e32 v4, 16, v0
	v_and_b32_e32 v0, 0xffff0000, v0
	v_mul_f32_e32 v181, 0.5, v0
	v_lshlrev_b32_e32 v0, 16, v1
	v_mul_f32_e32 v180, 0.5, v0
	v_and_b32_e32 v0, 0xffff0000, v1
	s_add_i32 s3, s1, -1
	s_add_i32 s5, s2, 1
	v_mul_f32_e32 v179, 0.5, v0
	v_lshlrev_b32_e32 v0, 16, v2
	s_min_i32 s5, s5, s3
	v_mul_f32_e32 v178, 0.5, v0
	v_and_b32_e32 v0, 0xffff0000, v2
	s_sub_i32 s6, s5, s2
	v_mul_f32_e32 v177, 0.5, v0
	v_lshlrev_b32_e32 v0, 16, v3
	s_ashr_i32 s7, s6, 31
	s_add_i32 s5, s2, 2
	v_mul_f32_e32 v176, 0.5, v0
	v_and_b32_e32 v0, 0xffff0000, v3
	s_lshl_b64 s[6:7], s[6:7], 11
	s_min_i32 s5, s5, s3
	v_mul_f32_e32 v175, 0.5, v0
	v_lshl_add_u64 v[0:1], v[142:143], 0, s[6:7]
	s_sub_i32 s6, s5, s2
	s_ashr_i32 s7, s6, 31
	s_add_i32 s5, s2, 3
	s_lshl_b64 s[6:7], s[6:7], 11
	s_min_i32 s5, s5, s3
	v_mov_b64_e32 v[100:101], v[188:189]
	v_mov_b64_e32 v[102:103], v[190:191]
	v_mov_b64_e32 v[96:97], v[192:193]
	v_mov_b64_e32 v[98:99], v[194:195]
	v_mov_b64_e32 v[92:93], v[196:197]
	v_mov_b64_e32 v[94:95], v[198:199]
	v_mov_b64_e32 v[88:89], v[200:201]
	v_mov_b64_e32 v[90:91], v[202:203]
	v_lshl_add_u64 v[0:1], v[142:143], 0, s[6:7]
	s_sub_i32 s6, s5, s2
	s_ashr_i32 s7, s6, 31
	s_lshl_b64 s[6:7], s[6:7], 11
	v_mov_b64_e32 v[84:85], v[204:205]
	v_mov_b64_e32 v[86:87], v[206:207]
	v_mov_b64_e32 v[80:81], v[208:209]
	v_mov_b64_e32 v[82:83], v[210:211]
	v_lshl_add_u64 v[0:1], v[142:143], 0, s[6:7]
	v_mov_b64_e32 v[76:77], v[220:221]
	v_mov_b64_e32 v[78:79], v[222:223]
	v_mov_b64_e32 v[72:73], v[224:225]
	v_mov_b64_e32 v[74:75], v[226:227]
	s_add_i32 s5, s2, 8
	v_mul_f32_e32 v158, 0.5, v16
	v_mul_f32_e32 v166, 0.5, v12
	v_mul_f32_e32 v174, 0.5, v8
	v_mul_f32_e32 v182, 0.5, v4
	s_cmp_gt_i32 s5, s1
	v_lshlrev_b32_e32 v146, 15, v29
	v_lshlrev_b32_e32 v144, 2, v28
	s_cbranch_scc1 .LBB0_711
	v_mov_b32_e32 v145, v128
	s_mul_i32 s5, s0, s4
	v_lshl_add_u64 v[0:1], v[140:141], 0, v[144:145]
	v_mov_b32_e32 v147, v128
	s_lshl_b32 s5, s5, 5
	v_lshl_add_u64 v[148:149], v[0:1], 0, v[146:147]
	s_mov_b32 s4, 5
	s_add_i32 s6, s5, 0xe0
